# all converter f32 weight loads (P2 background, P2-end, P9 too) carry sc1 besides nt
# baseline (speedup 1.0000x reference)
; __device__ __forceinline__ void cvt_load(CvtBuf& b, const CvtDesc& d, int lane) {
;     const float* p = d.W + (size_t)(d.k0 + 16 * (lane >> 5)) * d.ldw + d.n0 + 4 * (lane & 31);
; #pragma unroll
;     for (int i = 0; i < 16; ++i) b.v[i] = __builtin_nontemporal_load((const f32x4*)(p + (size_t)i * d.ldw));
; }
.LBB0_465:
	s_lshl_b32 s24, s38, 7
	s_lshl_b32 s11, s60, 7
	s_lshl_b32 s38, s62, 5
	s_and_b32 s11, s11, 0x780
	s_and_b32 s38, s38, 32
	s_or_b32 s11, s38, s11
	v_or_b32_e32 v2, s11, v201
	v_mul_u32_u24_e32 v2, s96, v2
	v_lshlrev_b32_e32 v2, 2, v2
	v_lshl_add_u64 v[36:37], s[6:7], 0, v[2:3]
	v_lshl_add_u64 v[36:37], s[24:25], 2, v[36:37]
	v_mov_b32_e32 v185, v3
	v_lshl_add_u64 v[36:37], v[36:37], 0, v[184:185]
	s_lshl_b32 s24, s96, 2
	v_lshl_add_u64 v[38:39], v[36:37], 0, s[24:25]
	global_load_dwordx4 v[108:111], v[36:37], off sc1 nt
	global_load_dwordx4 v[104:107], v[38:39], off sc1 nt
	v_lshl_add_u64 v[36:37], v[38:39], 0, s[24:25]
	v_lshl_add_u64 v[38:39], v[36:37], 0, s[24:25]
	global_load_dwordx4 v[156:159], v[36:37], off sc1 nt
	global_load_dwordx4 v[144:147], v[38:39], off sc1 nt
	v_lshl_add_u64 v[36:37], v[38:39], 0, s[24:25]
	v_lshl_add_u64 v[38:39], v[36:37], 0, s[24:25]
	global_load_dwordx4 v[152:155], v[36:37], off sc1 nt
	global_load_dwordx4 v[140:143], v[38:39], off sc1 nt
	v_lshl_add_u64 v[36:37], v[38:39], 0, s[24:25]
	v_lshl_add_u64 v[38:39], v[36:37], 0, s[24:25]
	global_load_dwordx4 v[136:139], v[36:37], off sc1 nt
	global_load_dwordx4 v[128:131], v[38:39], off sc1 nt
	v_lshl_add_u64 v[36:37], v[38:39], 0, s[24:25]
	global_load_dwordx4 v[116:119], v[36:37], off sc1 nt
	v_lshl_add_u64 v[36:37], v[36:37], 0, s[24:25]
	global_load_dwordx4 v[124:127], v[36:37], off sc1 nt
	v_lshl_add_u64 v[36:37], v[36:37], 0, s[24:25]
	global_load_dwordx4 v[132:135], v[36:37], off sc1 nt
	v_lshl_add_u64 v[36:37], v[36:37], 0, s[24:25]
	global_load_dwordx4 v[148:151], v[36:37], off sc1 nt
	v_lshl_add_u64 v[36:37], v[36:37], 0, s[24:25]
	global_load_dwordx4 v[112:115], v[36:37], off sc1 nt
	v_lshl_add_u64 v[36:37], v[36:37], 0, s[24:25]
	global_load_dwordx4 v[120:123], v[36:37], off sc1 nt
	v_lshl_add_u64 v[36:37], v[36:37], 0, s[24:25]
	global_load_dwordx4 v[96:99], v[36:37], off sc1 nt
	v_lshl_add_u64 v[36:37], v[36:37], 0, s[24:25]
	global_load_dwordx4 v[100:103], v[36:37], off sc1 nt
	s_mov_b32 s60, 2
	s_mov_b32 s38, 1

; __device__ __forceinline__ void cvt_load(CvtBuf& b, const CvtDesc& d, int lane) {
;     const float* p = d.W + (size_t)(d.k0 + 16 * (lane >> 5)) * d.ldw + d.n0 + 4 * (lane & 31);
; #pragma unroll
;     for (int i = 0; i < 16; ++i) b.v[i] = __builtin_nontemporal_load((const f32x4*)(p + (size_t)i * d.ldw));
; }
.LBB0_602:
	s_lshl_b32 s14, s38, 7
	s_lshl_b32 s11, s11, 7
	s_lshl_b32 s38, s10, 5
	s_and_b32 s11, s11, 0x780
	s_and_b32 s38, s38, 32
	s_or_b32 s11, s38, s11
	v_or_b32_e32 v34, s11, v171
	v_mul_u32_u24_e32 v34, s80, v34
	v_lshlrev_b32_e32 v82, 2, v34
	v_lshl_add_u64 v[34:35], s[6:7], 0, v[82:83]
	v_lshl_add_u64 v[34:35], s[14:15], 2, v[34:35]
	v_mov_b32_e32 v91, v83
	v_lshl_add_u64 v[34:35], v[34:35], 0, v[90:91]
	s_lshl_b32 s14, s80, 2
	v_lshl_add_u64 v[36:37], v[34:35], 0, s[14:15]
	global_load_dwordx4 v[108:111], v[34:35], off sc1 nt
	global_load_dwordx4 v[104:107], v[36:37], off sc1 nt
	v_lshl_add_u64 v[34:35], v[36:37], 0, s[14:15]
	v_lshl_add_u64 v[36:37], v[34:35], 0, s[14:15]
	global_load_dwordx4 v[156:159], v[34:35], off sc1 nt
	global_load_dwordx4 v[144:147], v[36:37], off sc1 nt
	v_lshl_add_u64 v[34:35], v[36:37], 0, s[14:15]
	v_lshl_add_u64 v[36:37], v[34:35], 0, s[14:15]
	global_load_dwordx4 v[152:155], v[34:35], off sc1 nt
	global_load_dwordx4 v[140:143], v[36:37], off sc1 nt
	v_lshl_add_u64 v[34:35], v[36:37], 0, s[14:15]
	v_lshl_add_u64 v[36:37], v[34:35], 0, s[14:15]
	global_load_dwordx4 v[136:139], v[34:35], off sc1 nt
	global_load_dwordx4 v[128:131], v[36:37], off sc1 nt
	v_lshl_add_u64 v[34:35], v[36:37], 0, s[14:15]
	global_load_dwordx4 v[116:119], v[34:35], off sc1 nt
	v_lshl_add_u64 v[34:35], v[34:35], 0, s[14:15]
	global_load_dwordx4 v[124:127], v[34:35], off sc1 nt
	v_lshl_add_u64 v[34:35], v[34:35], 0, s[14:15]
	global_load_dwordx4 v[132:135], v[34:35], off sc1 nt
	v_lshl_add_u64 v[34:35], v[34:35], 0, s[14:15]
	global_load_dwordx4 v[148:151], v[34:35], off sc1 nt
	v_lshl_add_u64 v[34:35], v[34:35], 0, s[14:15]
	global_load_dwordx4 v[112:115], v[34:35], off sc1 nt
	v_lshl_add_u64 v[34:35], v[34:35], 0, s[14:15]
	global_load_dwordx4 v[120:123], v[34:35], off sc1 nt
	v_lshl_add_u64 v[34:35], v[34:35], 0, s[14:15]
	global_load_dwordx4 v[96:99], v[34:35], off sc1 nt
	v_lshl_add_u64 v[34:35], v[34:35], 0, s[14:15]
	global_load_dwordx4 v[100:103], v[34:35], off sc1 nt
	s_mov_b32 s60, 2
	s_mov_b32 s38, 1

;     __device__ __forceinline__ CvtDesc desc(int qq) const { return cvt_desc(*F, item_of(qq), qq & 1, h); }
;     __device__ __forceinline__ void proc() { cvt_to_lds(buf, desc(q), img, gl, q & 1, h, F->lane); if (q & 1) fitem = item_of(q); ++q; }
;     __device__ __forceinline__ void flush() { if (fitem >= 0) { cvt_flush(cvt_desc(*F, fitem, 0, h), img, h, F->lane); fitem = -1; } }
; __device__ __forceinline__ CvtDesc cvt_desc(const Frame& F, int item, int sub2, int h) {
;     CvtDesc d; int kblk, nblk;
;     if (item < CVT_ITEMS1) { const int e = item >> 9, rem = item & 511; kblk = rem >> 5; nblk = rem & 31; d.W = F.w_mlp1 + (size_t)e * DM * 2 * DE; d.ldw = 2 * DE; d.WT = F.ws + WS_W1 + (size_t)e * 2 * DE * DM; d.map = 2; }
;     else { const int it = item - CVT_ITEMS1; const int e = it >> 8, rem = it & 255; kblk = rem >> 4; nblk = rem & 15; d.W = F.w_mlp2 + (size_t)e * DE * DM; d.ldw = DM; d.WT = F.ws + WS_W2 + (size_t)e * DM * DE; d.map = 0; }
;     d.n0 = nblk * 128; d.kb0 = kblk * 128; d.k0 = d.kb0 + 64 * h + 32 * sub2;
;     return d;
; }
; __device__ __forceinline__ void cvt_load(CvtBuf& b, const CvtDesc& d, int lane) {
;     const float* p = d.W + (size_t)(d.k0 + 16 * (lane >> 5)) * d.ldw + d.n0 + 4 * (lane & 31);
; #pragma unroll
;     for (int i = 0; i < 16; ++i) b.v[i] = __builtin_nontemporal_load((const f32x4*)(p + (size_t)i * d.ldw));
; }
;     __device__ __forceinline__ void drain() {
;         __syncthreads(); flush(); __syncthreads();
;         if (state != 0) { proc(); state = 0; if (fitem >= 0) { __syncthreads(); flush(); __syncthreads(); } }
;         if (q >= nq) { __syncthreads(); return; }
;         CvtBuf b2;
;         cvt_load(buf, desc(q), F->lane);
;         while (q < nq) {
.LBB0_687:
	s_lshl_b32 s5, s8, 7
	s_lshl_b32 s7, s10, 5
	s_and_b32 s5, s5, 0x780
	s_lshl_b32 s8, s49, 6
	s_and_b32 s7, s7, 32
	v_lshrrev_b32_e32 v1, 1, v0
	s_or_b32 s5, s7, s5
	v_and_or_b32 v1, v1, 16, s8
	v_or_b32_e32 v2, s5, v1
	v_mul_u32_u24_e32 v2, s6, v2
	v_lshlrev_b32_e32 v130, 2, v2
	v_mov_b32_e32 v131, 0
	s_lshl_b32 s4, s9, 7
	s_mov_b32 s5, 0
	v_lshl_add_u64 v[2:3], s[0:1], 0, v[130:131]
	v_and_b32_e32 v132, 0x7c, v176
	v_lshl_add_u64 v[2:3], s[4:5], 2, v[2:3]
	v_lshlrev_b32_e32 v130, 2, v132
	v_lshl_add_u64 v[10:11], v[2:3], 0, v[130:131]
	s_lshl_b32 s4, s6, 2
	v_lshl_add_u64 v[12:13], v[10:11], 0, s[4:5]
	v_lshl_add_u64 v[18:19], v[12:13], 0, s[4:5]
	v_lshl_add_u64 v[20:21], v[18:19], 0, s[4:5]
	v_lshl_add_u64 v[26:27], v[20:21], 0, s[4:5]
	v_lshl_add_u64 v[28:29], v[26:27], 0, s[4:5]
	v_lshl_add_u64 v[34:35], v[28:29], 0, s[4:5]
	v_lshl_add_u64 v[36:37], v[34:35], 0, s[4:5]
	v_lshl_add_u64 v[38:39], v[36:37], 0, s[4:5]
	v_lshl_add_u64 v[42:43], v[38:39], 0, s[4:5]
	v_lshl_add_u64 v[46:47], v[42:43], 0, s[4:5]
	v_lshl_add_u64 v[50:51], v[46:47], 0, s[4:5]
	v_lshl_add_u64 v[54:55], v[50:51], 0, s[4:5]
	v_lshl_add_u64 v[58:59], v[54:55], 0, s[4:5]
	v_lshl_add_u64 v[62:63], v[58:59], 0, s[4:5]
	global_load_dwordx4 v[2:5], v[10:11], off sc1 nt
	global_load_dwordx4 v[6:9], v[12:13], off sc1 nt
	s_nop 0
	global_load_dwordx4 v[10:13], v[18:19], off sc1 nt
	global_load_dwordx4 v[14:17], v[20:21], off sc1 nt
	s_nop 0
	global_load_dwordx4 v[18:21], v[26:27], off sc1 nt
	global_load_dwordx4 v[22:25], v[28:29], off sc1 nt
	s_nop 0
	global_load_dwordx4 v[26:29], v[34:35], off sc1 nt
	global_load_dwordx4 v[30:33], v[36:37], off sc1 nt
	s_lshl_b32 s0, s49, 8
	global_load_dwordx4 v[34:37], v[38:39], off sc1 nt
	s_add_i32 s11, s0, 0
	global_load_dwordx4 v[38:41], v[42:43], off sc1 nt
	s_add_u32 s34, s30, 0x50000000
	global_load_dwordx4 v[42:45], v[46:47], off sc1 nt
	s_addc_u32 s35, s31, 0
	global_load_dwordx4 v[46:49], v[50:51], off sc1 nt
	s_add_u32 s38, s30, 0x30000000
	global_load_dwordx4 v[50:53], v[54:55], off sc1 nt
	s_addc_u32 s39, s31, 0
	global_load_dwordx4 v[54:57], v[58:59], off sc1 nt
	v_lshlrev_b32_e32 v67, 9, v0
	global_load_dwordx4 v[58:61], v[62:63], off sc1 nt
	v_lshl_add_u64 v[62:63], v[62:63], 0, s[4:5]
	global_load_dwordx4 v[62:65], v[62:63], off sc1 nt
	s_bitcmp0_b32 s10, 0
	v_and_b32_e32 v67, 0x3e00, v67
	s_cselect_b64 s[6:7], -1, 0
	s_lshl_b32 s0, s49, 13
	v_add_u32_e32 v138, s50, v67
	v_lshrrev_b32_e32 v67, 3, v190
	v_lshlrev_b32_e32 v68, 4, v0
	s_add_i32 s0, s48, s0
	v_lshrrev_b32_e32 v66, 5, v190
	v_and_b32_e32 v134, 0x70, v68
	v_lshlrev_b32_e32 v68, 7, v67
	v_or_b32_e32 v142, s8, v67
	s_add_i32 s0, s0, 0
	v_lshlrev_b32_e32 v133, 6, v66
	v_lshl_or_b32 v141, s49, 2, v66
	v_or_b32_e32 v143, 24, v142
	v_add_u32_e32 v66, s0, v68
	v_or_b32_e32 v146, 16, v142
	v_or_b32_e32 v148, 8, v142
	v_and_b32_e32 v139, 7, v0
	v_mov_b32_e32 v135, v131
	v_and_b32_e32 v140, 0x80, v68
	v_lshrrev_b32_e32 v144, 2, v143
	v_add_u32_e32 v145, 0x16000, v66
	v_lshrrev_b32_e32 v147, 2, v146
	v_lshrrev_b32_e32 v149, 2, v148
	v_lshrrev_b32_e32 v150, 2, v142
	v_mov_b32_e32 v151, 0x42800000
	s_branch .LBB0_689

;     __device__ __forceinline__ CvtDesc desc(int qq) const { return cvt_desc(*F, item_of(qq), qq & 1, h); }
;     __device__ __forceinline__ void flush() { if (fitem >= 0) { cvt_flush(cvt_desc(*F, fitem, 0, h), img, h, F->lane); fitem = -1; } }
; __device__ __forceinline__ void cvt_load(CvtBuf& b, const CvtDesc& d, int lane) {
;     const float* p = d.W + (size_t)(d.k0 + 16 * (lane >> 5)) * d.ldw + d.n0 + 4 * (lane & 31);
; #pragma unroll
;     for (int i = 0; i < 16; ++i) b.v[i] = __builtin_nontemporal_load((const f32x4*)(p + (size_t)i * d.ldw));
; }
;     __device__ __forceinline__ void drain() {
;     ...
;         while (q < nq) {
;             if (q + 1 < nq) cvt_load(b2, desc(q + 1), F->lane);
;             cvt_to_lds(buf, desc(q), img, gl, q & 1, h, F->lane); if (q & 1) fitem = item_of(q); ++q;
;             if (fitem >= 0) { __syncthreads(); flush(); __syncthreads(); }
;             if (q >= nq) break;
;             if (q + 1 < nq) cvt_load(buf, desc(q + 1), F->lane);
;             cvt_to_lds(b2, desc(q), img, gl, q & 1, h, F->lane); if (q & 1) fitem = item_of(q); ++q;
.LBB0_694:
	s_lshl_b32 s15, s36, 7
	s_lshl_b32 s36, s40, 5
	s_and_b32 s15, s15, 0x780
	s_and_b32 s36, s36, 32
	s_or_b32 s15, s36, s15
	v_or_b32_e32 v66, s15, v1
	v_mul_u32_u24_e32 v66, s14, v66
	v_lshlrev_b32_e32 v130, 2, v66
	s_lshl_b32 s4, s37, 7
	v_lshl_add_u64 v[66:67], s[0:1], 0, v[130:131]
	v_lshl_add_u64 v[66:67], s[4:5], 2, v[66:67]
	v_lshlrev_b32_e32 v130, 2, v132
	v_lshl_add_u64 v[66:67], v[66:67], 0, v[130:131]
	s_lshl_b32 s4, s14, 2
	v_lshl_add_u64 v[74:75], v[66:67], 0, s[4:5]
	global_load_dwordx4 v[70:73], v[66:67], off sc1 nt
	s_nop 0
	global_load_dwordx4 v[66:69], v[74:75], off sc1 nt
	v_lshl_add_u64 v[74:75], v[74:75], 0, s[4:5]
	v_lshl_add_u64 v[82:83], v[74:75], 0, s[4:5]
	global_load_dwordx4 v[78:81], v[74:75], off sc1 nt
	s_nop 0
	global_load_dwordx4 v[74:77], v[82:83], off sc1 nt
	v_lshl_add_u64 v[82:83], v[82:83], 0, s[4:5]
	v_lshl_add_u64 v[90:91], v[82:83], 0, s[4:5]
	global_load_dwordx4 v[86:89], v[82:83], off sc1 nt
	s_nop 0
	global_load_dwordx4 v[82:85], v[90:91], off sc1 nt
	v_lshl_add_u64 v[90:91], v[90:91], 0, s[4:5]
	v_lshl_add_u64 v[98:99], v[90:91], 0, s[4:5]
	v_lshl_add_u64 v[102:103], v[98:99], 0, s[4:5]
	v_lshl_add_u64 v[106:107], v[102:103], 0, s[4:5]
	v_lshl_add_u64 v[110:111], v[106:107], 0, s[4:5]
	v_lshl_add_u64 v[114:115], v[110:111], 0, s[4:5]
	v_lshl_add_u64 v[118:119], v[114:115], 0, s[4:5]
	v_lshl_add_u64 v[122:123], v[118:119], 0, s[4:5]
	v_lshl_add_u64 v[126:127], v[122:123], 0, s[4:5]
	global_load_dwordx4 v[94:97], v[90:91], off sc1 nt
	s_nop 0
	global_load_dwordx4 v[90:93], v[98:99], off sc1 nt
	s_nop 0
	global_load_dwordx4 v[98:101], v[102:103], off sc1 nt
	s_nop 0
	global_load_dwordx4 v[102:105], v[106:107], off sc1 nt
	s_nop 0
	global_load_dwordx4 v[106:109], v[110:111], off sc1 nt
	s_nop 0
	global_load_dwordx4 v[110:113], v[114:115], off sc1 nt
	s_nop 0
	global_load_dwordx4 v[114:117], v[118:119], off sc1 nt
	s_nop 0
	global_load_dwordx4 v[118:121], v[122:123], off sc1 nt
	s_nop 0
	global_load_dwordx4 v[122:125], v[126:127], off sc1 nt
	v_lshl_add_u64 v[126:127], v[126:127], 0, s[4:5]
	global_load_dwordx4 v[126:129], v[126:127], off sc1 nt

;     __device__ __forceinline__ CvtDesc desc(int qq) const { return cvt_desc(*F, item_of(qq), qq & 1, h); }
;     __device__ __forceinline__ void flush() { if (fitem >= 0) { cvt_flush(cvt_desc(*F, fitem, 0, h), img, h, F->lane); fitem = -1; } }
; __device__ __forceinline__ void cvt_load(CvtBuf& b, const CvtDesc& d, int lane) {
;     const float* p = d.W + (size_t)(d.k0 + 16 * (lane >> 5)) * d.ldw + d.n0 + 4 * (lane & 31);
; #pragma unroll
;     for (int i = 0; i < 16; ++i) b.v[i] = __builtin_nontemporal_load((const f32x4*)(p + (size_t)i * d.ldw));
; }
;     __device__ __forceinline__ void drain() {
;     ...
;         while (q < nq) {
;             if (q + 1 < nq) cvt_load(b2, desc(q + 1), F->lane);
;             cvt_to_lds(buf, desc(q), img, gl, q & 1, h, F->lane); if (q & 1) fitem = item_of(q); ++q;
;             if (fitem >= 0) { __syncthreads(); flush(); __syncthreads(); }
;             if (q >= nq) break;
;             if (q + 1 < nq) cvt_load(buf, desc(q + 1), F->lane);
;             cvt_to_lds(b2, desc(q), img, gl, q & 1, h, F->lane); if (q & 1) fitem = item_of(q); ++q;
.LBB0_709:
	s_lshl_b32 s15, s36, 7
	s_and_b32 s15, s15, 0x780
	v_or_b32_e32 v2, s15, v1
	v_or_b32_e32 v2, s41, v2
	v_mul_u32_u24_e32 v2, s14, v2
	v_lshlrev_b32_e32 v130, 2, v2
	s_lshl_b32 s4, s37, 7
	v_lshl_add_u64 v[2:3], s[0:1], 0, v[130:131]
	v_lshl_add_u64 v[2:3], s[4:5], 2, v[2:3]
	v_lshlrev_b32_e32 v130, 2, v132
	v_lshl_add_u64 v[2:3], v[2:3], 0, v[130:131]
	s_lshl_b32 s4, s14, 2
	v_lshl_add_u64 v[10:11], v[2:3], 0, s[4:5]
	global_load_dwordx4 v[2:5], v[2:3], off sc1 nt
	s_nop 0
	global_load_dwordx4 v[6:9], v[10:11], off sc1 nt
	v_lshl_add_u64 v[10:11], v[10:11], 0, s[4:5]
	v_lshl_add_u64 v[18:19], v[10:11], 0, s[4:5]
	global_load_dwordx4 v[10:13], v[10:11], off sc1 nt
	s_nop 0
	global_load_dwordx4 v[14:17], v[18:19], off sc1 nt
	v_lshl_add_u64 v[18:19], v[18:19], 0, s[4:5]
	v_lshl_add_u64 v[26:27], v[18:19], 0, s[4:5]
	global_load_dwordx4 v[18:21], v[18:19], off sc1 nt
	s_nop 0
	global_load_dwordx4 v[22:25], v[26:27], off sc1 nt
	v_lshl_add_u64 v[26:27], v[26:27], 0, s[4:5]
	v_lshl_add_u64 v[34:35], v[26:27], 0, s[4:5]
	v_lshl_add_u64 v[38:39], v[34:35], 0, s[4:5]
	v_lshl_add_u64 v[42:43], v[38:39], 0, s[4:5]
	v_lshl_add_u64 v[46:47], v[42:43], 0, s[4:5]
	v_lshl_add_u64 v[50:51], v[46:47], 0, s[4:5]
	v_lshl_add_u64 v[54:55], v[50:51], 0, s[4:5]
	v_lshl_add_u64 v[58:59], v[54:55], 0, s[4:5]
	v_lshl_add_u64 v[62:63], v[58:59], 0, s[4:5]
	global_load_dwordx4 v[26:29], v[26:27], off sc1 nt
	s_nop 0
	global_load_dwordx4 v[30:33], v[34:35], off sc1 nt
	s_nop 0
	global_load_dwordx4 v[34:37], v[38:39], off sc1 nt
	s_nop 0
	global_load_dwordx4 v[38:41], v[42:43], off sc1 nt
	s_nop 0
	global_load_dwordx4 v[42:45], v[46:47], off sc1 nt
	s_nop 0
	global_load_dwordx4 v[46:49], v[50:51], off sc1 nt
	s_nop 0
	global_load_dwordx4 v[50:53], v[54:55], off sc1 nt
	s_nop 0
	global_load_dwordx4 v[54:57], v[58:59], off sc1 nt
	s_nop 0
	global_load_dwordx4 v[58:61], v[62:63], off sc1 nt
	v_lshl_add_u64 v[62:63], v[62:63], 0, s[4:5]
	global_load_dwordx4 v[62:65], v[62:63], off sc1 nt
	s_waitcnt vmcnt(16)

;     __device__ __forceinline__ void init(const Frame& F_, int first_item, int n_items) { init(F_, first_item, n_items, F_.vcu, F_.G); }
; __device__ __forceinline__ CvtDesc cvt_desc(const Frame& F, int item, int sub2, int h) {
;     CvtDesc d; int kblk, nblk;
;     if (item < CVT_ITEMS1) { const int e = item >> 9, rem = item & 511; kblk = rem >> 5; nblk = rem & 31; d.W = F.w_mlp1 + (size_t)e * DM * 2 * DE; d.ldw = 2 * DE; d.WT = F.ws + WS_W1 + (size_t)e * 2 * DE * DM; d.map = 2; }
;     else { const int it = item - CVT_ITEMS1; const int e = it >> 8, rem = it & 255; kblk = rem >> 4; nblk = rem & 15; d.W = F.w_mlp2 + (size_t)e * DE * DM; d.ldw = DM; d.WT = F.ws + WS_W2 + (size_t)e * DM * DE; d.map = 0; }
;     d.n0 = nblk * 128; d.kb0 = kblk * 128; d.k0 = d.kb0 + 64 * h + 32 * sub2;
;     return d;
; }
; __device__ __forceinline__ void cvt_load(CvtBuf& b, const CvtDesc& d, int lane) {
;     const float* p = d.W + (size_t)(d.k0 + 16 * (lane >> 5)) * d.ldw + d.n0 + 4 * (lane & 31);
; #pragma unroll
;     for (int i = 0; i < 16; ++i) b.v[i] = __builtin_nontemporal_load((const f32x4*)(p + (size_t)i * d.ldw));
; }
; __global__ void __launch_bounds__(NTHREADS, 2) mk_fwd(Args args) {
;     ...
;         if (F.G == 256) {
;             const int rem = total & 255; int first = rem; nconv = 256 - rem;
;             if (nconv < 64) { first = 0; nconv = 256; }
;             nparts = 2;
;             if (F.vcu >= first) {
;                 Bg bg; bg.init(F, CVT_ITEMS - CVT_P9_ITEMS, CVT_P9_ITEMS, F.vcu - first, nconv); bg.drain();
.LBB0_1275:
	s_cmp_lg_u32 s12, 0
	s_mov_b32 s1, 0
	s_barrier
	s_barrier
	s_cbranch_scc0 .LBB0_1395
	v_readlane_b32 s0, v254, 47
	s_lshl_b32 s0, s0, 13
	s_and_b32 s45, s0, 0x7fffc000
	v_readlane_b32 s0, v254, 8
	s_bfe_u32 s47, s0, 0x10006
	s_add_i32 s0, s10, 0xffffc000
	v_readlane_b32 s56, v254, 0
	s_add_i32 s46, 0, 0x16000
	s_lshr_b32 s0, s0, 8
	v_readlane_b32 s58, v254, 2
	v_readlane_b32 s59, v254, 3
	s_add_i32 s42, s46, s45
	s_lshl_b64 s[8:9], s[0:1], 24
	s_mov_b64 s[14:15], s[58:59]
	s_add_u32 s8, s14, s8
	s_addc_u32 s9, s15, s9
	s_lshl_b32 s14, s10, 3
	v_lshrrev_b32_e32 v1, 1, v0
	s_and_b32 s0, s14, 0x780
	v_and_b32_e32 v1, 16, v1
	s_lshl_b32 s44, s47, 6
	v_or_b32_e32 v2, s0, v1
	v_or_b32_e32 v2, s44, v2
	v_lshlrev_b32_e32 v130, 13, v2
	v_mov_b32_e32 v131, 0
	s_lshl_b32 s0, s10, 9
	v_lshlrev_b32_e32 v4, 2, v0
	v_lshl_add_u64 v[2:3], s[8:9], 0, v[130:131]
	s_and_b32 s0, s0, 0x1e00
	v_and_b32_e32 v132, 0x7c, v4
	v_lshl_add_u64 v[2:3], v[2:3], 0, s[0:1]
	v_lshlrev_b32_e32 v130, 2, v132
	v_lshl_add_u64 v[58:59], v[2:3], 0, v[130:131]
	s_movk_i32 s15, 0x2000
	v_add_co_u32_e32 v10, vcc, s15, v58
	s_movk_i32 s16, 0x4000
	s_nop 0
	v_addc_co_u32_e32 v11, vcc, 0, v59, vcc
	v_add_co_u32_e32 v18, vcc, s16, v58
	s_movk_i32 s17, 0x6000
	s_nop 0
	v_addc_co_u32_e32 v19, vcc, 0, v59, vcc
	v_add_co_u32_e32 v20, vcc, s17, v58
	s_mov_b32 s18, 0x8000
	s_nop 0
	v_addc_co_u32_e32 v21, vcc, 0, v59, vcc
	global_load_dwordx4 v[2:5], v[58:59], off sc1 nt
	global_load_dwordx4 v[6:9], v[10:11], off sc1 nt
	s_nop 0
	global_load_dwordx4 v[10:13], v[18:19], off sc1 nt
	global_load_dwordx4 v[14:17], v[20:21], off sc1 nt
	v_add_co_u32_e32 v18, vcc, s18, v58
	s_mov_b32 s19, 0xa000
	s_nop 0
	v_addc_co_u32_e32 v19, vcc, 0, v59, vcc
	v_add_co_u32_e32 v22, vcc, s19, v58
	s_mov_b32 s20, 0xc000
	s_nop 0
	v_addc_co_u32_e32 v23, vcc, 0, v59, vcc
	v_add_co_u32_e32 v26, vcc, s20, v58
	s_mov_b32 s36, 0xe000
	s_nop 0
	v_addc_co_u32_e32 v27, vcc, 0, v59, vcc
	v_add_co_u32_e32 v30, vcc, s36, v58
	s_mov_b32 s37, 0x10000
	s_nop 0
	v_addc_co_u32_e32 v31, vcc, 0, v59, vcc
	v_add_co_u32_e32 v34, vcc, s37, v58
	s_mov_b32 s38, 0x12000
	s_nop 0
	v_addc_co_u32_e32 v35, vcc, 0, v59, vcc
	v_add_co_u32_e32 v38, vcc, s38, v58
	s_mov_b32 s39, 0x14000
	s_nop 0
	v_addc_co_u32_e32 v39, vcc, 0, v59, vcc
	v_add_co_u32_e32 v42, vcc, s39, v58
	s_mov_b32 s13, 0x16000
	s_nop 0
	v_addc_co_u32_e32 v43, vcc, 0, v59, vcc
	v_add_co_u32_e32 v46, vcc, s13, v58
	s_mov_b32 s40, 0x18000
	s_nop 0
	v_addc_co_u32_e32 v47, vcc, 0, v59, vcc
	v_add_co_u32_e32 v50, vcc, s40, v58
	s_mov_b32 s0, 0x1a000
	s_nop 0
	v_addc_co_u32_e32 v51, vcc, 0, v59, vcc
	v_add_co_u32_e32 v54, vcc, s0, v58
	s_mov_b32 s0, 0x1c000
	s_nop 0
	v_addc_co_u32_e32 v55, vcc, 0, v59, vcc
	v_add_co_u32_e32 v60, vcc, s0, v58
	s_mov_b32 s0, 0x1e000
	s_nop 0
	v_addc_co_u32_e32 v61, vcc, 0, v59, vcc
	v_add_co_u32_e32 v62, vcc, s0, v58
	global_load_dwordx4 v[18:21], v[18:19], off sc1 nt
	s_nop 0
	global_load_dwordx4 v[22:25], v[22:23], off sc1 nt
	v_addc_co_u32_e32 v63, vcc, 0, v59, vcc
	global_load_dwordx4 v[26:29], v[26:27], off sc1 nt
	s_nop 0
	global_load_dwordx4 v[30:33], v[30:31], off sc1 nt
	s_nop 0
	global_load_dwordx4 v[34:37], v[34:35], off sc1 nt
	s_nop 0
	global_load_dwordx4 v[38:41], v[38:39], off sc1 nt
	s_nop 0
	global_load_dwordx4 v[42:45], v[42:43], off sc1 nt
	s_nop 0
	global_load_dwordx4 v[46:49], v[46:47], off sc1 nt
	s_nop 0
	global_load_dwordx4 v[50:53], v[50:51], off sc1 nt
	s_nop 0
	global_load_dwordx4 v[54:57], v[54:55], off sc1 nt
	s_nop 0
	global_load_dwordx4 v[58:61], v[60:61], off sc1 nt
	s_nop 0
	global_load_dwordx4 v[62:65], v[62:63], off sc1 nt
	v_lshrrev_b32_e32 v66, 5, v190
	s_lshl_b32 s0, s47, 2
	v_and_b32_e32 v69, 7, v0
	v_or_b32_e32 v67, s0, v66
	v_bitop3_b32 v66, s0, v69, v66 bitop3:0x36
	s_lshl_b32 s0, s52, 2
	v_lshlrev_b32_e32 v68, 9, v0
	s_add_i32 s5, s5, s0
	s_lshl_b32 s0, s4, 2
	v_and_b32_e32 v68, 0x3e00, v68
	s_sub_i32 s0, s5, s0
	v_add_u32_e32 v68, s42, v68
	v_lshlrev_b32_e32 v70, 4, v66
	v_lshrrev_b32_e32 v71, 3, v190
	v_lshlrev_b32_e32 v66, 4, v0
	s_add_i32 s42, s0, 0x1800
	s_lshl_b32 s0, s47, 13
	v_and_b32_e32 v130, 0x70, v66
	v_bitop3_b32 v66, v67, v69, 2 bitop3:0x36
	v_or_b32_e32 v133, s44, v71
	s_or_b32 s0, s45, s0
	v_readlane_b32 s57, v254, 1
	v_lshlrev_b32_e32 v69, 4, v66
	v_lshl_add_u64 v[66:67], s[30:31], 0, v[130:131]
	s_mov_b64 s[8:9], 0x50000000
	v_or_b32_e32 v144, 24, v133
	s_add_i32 s46, s46, s0
	v_or_b32_e32 v147, 16, v133
	v_or_b32_e32 v149, 8, v133
	s_lshl_b32 s41, s10, 7
	v_or_b32_e32 v1, s44, v1
	v_lshl_add_u64 v[134:135], v[66:67], 0, s[8:9]
	s_lshl_b32 s43, s53, 5
	s_lshl_b32 s44, s53, 9
	v_lshrrev_b32_e32 v145, 2, v144
	v_lshl_add_u32 v146, v71, 7, s46
	v_lshrrev_b32_e32 v148, 2, v147
	v_lshrrev_b32_e32 v150, 2, v149
	v_lshrrev_b32_e32 v151, 2, v133
	s_mov_b32 s45, 0x40000
	s_mov_b32 s46, 0x42000
	s_mov_b32 s47, 0x44000
	s_mov_b32 s48, 0x46000
	s_mov_b32 s49, 0x48000
	s_mov_b32 s50, 0x4a000
	s_mov_b32 s51, 0x4c000
	s_mov_b32 s54, 0x4e000
	s_mov_b32 s55, 0x50000
	s_mov_b32 s56, 0x52000
	s_mov_b32 s57, 0x54000
	s_mov_b32 s58, 0x56000
	v_add_u32_e32 v152, v68, v70
	v_add_u32_e32 v153, v68, v69
	s_mov_b32 s59, 0
	v_readlane_b32 s60, v254, 4
	v_readlane_b32 s61, v254, 5
	v_readlane_b32 s62, v254, 6
	v_readlane_b32 s63, v254, 7
	s_branch .LBB0_1278

;     __device__ __forceinline__ CvtDesc desc(int qq) const { return cvt_desc(*F, item_of(qq), qq & 1, h); }
;     __device__ __forceinline__ void flush() { if (fitem >= 0) { cvt_flush(cvt_desc(*F, fitem, 0, h), img, h, F->lane); fitem = -1; } }
; __device__ __forceinline__ void cvt_load(CvtBuf& b, const CvtDesc& d, int lane) {
;     const float* p = d.W + (size_t)(d.k0 + 16 * (lane >> 5)) * d.ldw + d.n0 + 4 * (lane & 31);
; #pragma unroll
;     for (int i = 0; i < 16; ++i) b.v[i] = __builtin_nontemporal_load((const f32x4*)(p + (size_t)i * d.ldw));
; }
;     __device__ __forceinline__ void drain() {
;     ...
;         while (q < nq) {
;             if (q + 1 < nq) cvt_load(b2, desc(q + 1), F->lane);
;             cvt_to_lds(buf, desc(q), img, gl, q & 1, h, F->lane); if (q & 1) fitem = item_of(q); ++q;
;             if (fitem >= 0) { __syncthreads(); flush(); __syncthreads(); }
;             if (q >= nq) break;
;             if (q + 1 < nq) cvt_load(buf, desc(q + 1), F->lane);
;             cvt_to_lds(b2, desc(q), img, gl, q & 1, h, F->lane); if (q & 1) fitem = item_of(q); ++q;
.Ldr9_goA:
	s_lshr_b32 s0, s59, 1
	s_mul_i32 s0, s0, s11
	s_add_i32 s60, s0, s10
	s_add_i32 s0, s60, 0xffffc000
	v_readlane_b32 s64, v254, 0
	s_lshr_b32 s0, s0, 8
	v_readlane_b32 s66, v254, 2
	v_readlane_b32 s67, v254, 3
	s_lshl_b64 s[8:9], s[0:1], 24
	s_mov_b64 s[22:23], s[66:67]
	s_add_u32 s8, s22, s8
	s_addc_u32 s9, s23, s9
	s_lshl_b32 s0, s60, 3
	s_and_b32 s0, s0, 0x780
	v_or_b32_e32 v66, s0, v1
	v_lshlrev_b32_e32 v130, 13, v66
	s_lshl_b32 s0, s60, 9
	v_lshl_add_u64 v[66:67], s[8:9], 0, v[130:131]
	s_and_b32 s0, s0, 0x1e00
	v_lshl_add_u64 v[66:67], v[66:67], 0, s[0:1]
	v_lshlrev_b32_e32 v130, 2, v132
	v_lshl_add_u64 v[122:123], v[66:67], 0, v[130:131]
	v_add_co_u32_e32 v66, vcc, s45, v122
	v_readlane_b32 s65, v254, 1
	s_nop 0
	v_addc_co_u32_e32 v67, vcc, 0, v123, vcc
	v_add_co_u32_e32 v70, vcc, s46, v122
	v_readlane_b32 s68, v254, 4
	s_nop 0
	v_addc_co_u32_e32 v71, vcc, 0, v123, vcc
	v_add_co_u32_e32 v74, vcc, s47, v122
	global_load_dwordx4 v[66:69], v[66:67], off sc1 nt
	s_nop 0
	global_load_dwordx4 v[70:73], v[70:71], off sc1 nt
	v_addc_co_u32_e32 v75, vcc, 0, v123, vcc
	v_add_co_u32_e32 v78, vcc, s48, v122
	v_readlane_b32 s69, v254, 5
	s_nop 0
	v_addc_co_u32_e32 v79, vcc, 0, v123, vcc
	v_add_co_u32_e32 v82, vcc, s49, v122
	global_load_dwordx4 v[74:77], v[74:75], off sc1 nt
	s_nop 0
	global_load_dwordx4 v[78:81], v[78:79], off sc1 nt
	v_addc_co_u32_e32 v83, vcc, 0, v123, vcc
	v_add_co_u32_e32 v86, vcc, s50, v122
	v_readlane_b32 s70, v254, 6
	s_nop 0
	v_addc_co_u32_e32 v87, vcc, 0, v123, vcc
	v_add_co_u32_e32 v90, vcc, s51, v122
	global_load_dwordx4 v[82:85], v[82:83], off sc1 nt
	s_nop 0
	global_load_dwordx4 v[86:89], v[86:87], off sc1 nt
	v_addc_co_u32_e32 v91, vcc, 0, v123, vcc
	v_add_co_u32_e32 v94, vcc, s54, v122
	v_readlane_b32 s71, v254, 7
	s_nop 0
	v_addc_co_u32_e32 v95, vcc, 0, v123, vcc
	v_add_co_u32_e32 v98, vcc, s55, v122
	global_load_dwordx4 v[90:93], v[90:91], off sc1 nt
	s_nop 0
	global_load_dwordx4 v[94:97], v[94:95], off sc1 nt
	v_addc_co_u32_e32 v99, vcc, 0, v123, vcc
	v_add_co_u32_e32 v102, vcc, s56, v122
	s_nop 1
	v_addc_co_u32_e32 v103, vcc, 0, v123, vcc
	v_add_co_u32_e32 v106, vcc, s57, v122
	global_load_dwordx4 v[98:101], v[98:99], off sc1 nt
	s_nop 0
	global_load_dwordx4 v[102:105], v[102:103], off sc1 nt
	v_addc_co_u32_e32 v107, vcc, 0, v123, vcc
	v_add_co_u32_e32 v110, vcc, s58, v122
	s_nop 1
	v_addc_co_u32_e32 v111, vcc, 0, v123, vcc
	v_add_co_u32_e32 v114, vcc, 0x58000, v122
	global_load_dwordx4 v[106:109], v[106:107], off sc1 nt
	s_nop 0
	global_load_dwordx4 v[110:113], v[110:111], off sc1 nt
	v_addc_co_u32_e32 v115, vcc, 0, v123, vcc
	v_add_co_u32_e32 v118, vcc, 0x5a000, v122
	s_nop 1
	v_addc_co_u32_e32 v119, vcc, 0, v123, vcc
	v_add_co_u32_e32 v124, vcc, 0x5c000, v122
	global_load_dwordx4 v[114:117], v[114:115], off sc1 nt
	s_nop 0
	global_load_dwordx4 v[118:121], v[118:119], off sc1 nt
	v_addc_co_u32_e32 v125, vcc, 0, v123, vcc
	v_add_co_u32_e32 v126, vcc, 0x5e000, v122
	s_nop 1
	v_addc_co_u32_e32 v127, vcc, 0, v123, vcc
	global_load_dwordx4 v[122:125], v[124:125], off sc1 nt
	s_nop 0
	global_load_dwordx4 v[126:129], v[126:127], off sc1 nt

;     __device__ __forceinline__ CvtDesc desc(int qq) const { return cvt_desc(*F, item_of(qq), qq & 1, h); }
;     __device__ __forceinline__ void flush() { if (fitem >= 0) { cvt_flush(cvt_desc(*F, fitem, 0, h), img, h, F->lane); fitem = -1; } }
; __device__ __forceinline__ void cvt_load(CvtBuf& b, const CvtDesc& d, int lane) {
;     const float* p = d.W + (size_t)(d.k0 + 16 * (lane >> 5)) * d.ldw + d.n0 + 4 * (lane & 31);
; #pragma unroll
;     for (int i = 0; i < 16; ++i) b.v[i] = __builtin_nontemporal_load((const f32x4*)(p + (size_t)i * d.ldw));
; }
;     __device__ __forceinline__ void drain() {
;     ...
;         while (q < nq) {
;             if (q + 1 < nq) cvt_load(b2, desc(q + 1), F->lane);
;             cvt_to_lds(buf, desc(q), img, gl, q & 1, h, F->lane); if (q & 1) fitem = item_of(q); ++q;
;             if (fitem >= 0) { __syncthreads(); flush(); __syncthreads(); }
;             if (q >= nq) break;
;             if (q + 1 < nq) cvt_load(buf, desc(q + 1), F->lane);
;             cvt_to_lds(b2, desc(q), img, gl, q & 1, h, F->lane); if (q & 1) fitem = item_of(q); ++q;
.Ldr9_goB:
	s_lshr_b32 s0, s59, 1
	s_mul_i32 s0, s0, s11
	s_add_i32 s60, s0, s10
	s_add_i32 s0, s60, 0xffffc000
	v_readlane_b32 s64, v254, 0
	s_lshr_b32 s0, s0, 8
	v_readlane_b32 s66, v254, 2
	v_readlane_b32 s67, v254, 3
	s_lshl_b64 s[8:9], s[0:1], 24
	s_mov_b64 s[22:23], s[66:67]
	s_add_u32 s8, s22, s8
	s_addc_u32 s9, s23, s9
	s_lshl_b32 s0, s60, 3
	s_and_b32 s0, s0, 0x780
	v_or_b32_e32 v2, s0, v1
	v_lshlrev_b32_e32 v130, 13, v2
	s_lshl_b32 s0, s60, 9
	v_lshl_add_u64 v[2:3], s[8:9], 0, v[130:131]
	s_and_b32 s0, s0, 0x1e00
	v_lshl_add_u64 v[2:3], v[2:3], 0, s[0:1]
	v_lshlrev_b32_e32 v130, 2, v132
	v_lshl_add_u64 v[58:59], v[2:3], 0, v[130:131]
	v_add_co_u32_e32 v6, vcc, s15, v58
	v_readlane_b32 s65, v254, 1
	s_nop 0
	v_addc_co_u32_e32 v7, vcc, 0, v59, vcc
	v_add_co_u32_e32 v10, vcc, s16, v58
	global_load_dwordx4 v[2:5], v[58:59], off sc1 nt
	s_nop 0
	global_load_dwordx4 v[6:9], v[6:7], off sc1 nt
	v_addc_co_u32_e32 v11, vcc, 0, v59, vcc
	v_add_co_u32_e32 v14, vcc, s17, v58
	v_readlane_b32 s68, v254, 4
	s_nop 0
	v_addc_co_u32_e32 v15, vcc, 0, v59, vcc
	v_add_co_u32_e32 v18, vcc, s18, v58
	global_load_dwordx4 v[10:13], v[10:11], off sc1 nt
	s_nop 0
	global_load_dwordx4 v[14:17], v[14:15], off sc1 nt
	v_addc_co_u32_e32 v19, vcc, 0, v59, vcc
	v_add_co_u32_e32 v22, vcc, s19, v58
	v_readlane_b32 s69, v254, 5
	s_nop 0
	v_addc_co_u32_e32 v23, vcc, 0, v59, vcc
	v_add_co_u32_e32 v26, vcc, s20, v58
	global_load_dwordx4 v[18:21], v[18:19], off sc1 nt
	s_nop 0
	global_load_dwordx4 v[22:25], v[22:23], off sc1 nt
	v_addc_co_u32_e32 v27, vcc, 0, v59, vcc
	v_add_co_u32_e32 v30, vcc, s36, v58
	v_readlane_b32 s70, v254, 6
	s_nop 0
	v_addc_co_u32_e32 v31, vcc, 0, v59, vcc
	v_add_co_u32_e32 v34, vcc, s37, v58
	global_load_dwordx4 v[26:29], v[26:27], off sc1 nt
	s_nop 0
	global_load_dwordx4 v[30:33], v[30:31], off sc1 nt
	v_addc_co_u32_e32 v35, vcc, 0, v59, vcc
	v_add_co_u32_e32 v38, vcc, s38, v58
	v_readlane_b32 s71, v254, 7
	s_nop 0
	v_addc_co_u32_e32 v39, vcc, 0, v59, vcc
	v_add_co_u32_e32 v42, vcc, s39, v58
	global_load_dwordx4 v[34:37], v[34:35], off sc1 nt
	s_nop 0
	global_load_dwordx4 v[38:41], v[38:39], off sc1 nt
	v_addc_co_u32_e32 v43, vcc, 0, v59, vcc
	v_add_co_u32_e32 v46, vcc, s13, v58
	s_nop 1
	v_addc_co_u32_e32 v47, vcc, 0, v59, vcc
	v_add_co_u32_e32 v50, vcc, s40, v58
	global_load_dwordx4 v[42:45], v[42:43], off sc1 nt
	s_nop 0
	global_load_dwordx4 v[46:49], v[46:47], off sc1 nt
	v_addc_co_u32_e32 v51, vcc, 0, v59, vcc
	v_add_co_u32_e32 v54, vcc, 0x1a000, v58
	s_nop 1
	v_addc_co_u32_e32 v55, vcc, 0, v59, vcc
	v_add_co_u32_e32 v60, vcc, 0x1c000, v58
	global_load_dwordx4 v[50:53], v[50:51], off sc1 nt
	s_nop 0
	global_load_dwordx4 v[54:57], v[54:55], off sc1 nt
	v_addc_co_u32_e32 v61, vcc, 0, v59, vcc
	v_add_co_u32_e32 v62, vcc, 0x1e000, v58
	s_nop 1
	v_addc_co_u32_e32 v63, vcc, 0, v59, vcc
	global_load_dwordx4 v[58:61], v[60:61], off sc1 nt
	s_nop 0
	global_load_dwordx4 v[62:65], v[62:63], off sc1 nt
	s_waitcnt vmcnt(16)
